# adds: sort HIST loads batched; DOWN gemm counted waits past epilogue stores, C=0 first MFMA, dead fp8 cvt inits removed
# speedup vs baseline: 1.0103x; 1.0103x over previous
; __device__ __forceinline__ void lds_barrier() { asm volatile("s_waitcnt lgkmcnt(0)" ::: "memory"); __builtin_amdgcn_s_barrier(); asm volatile("" ::: "memory"); }
; __device__ __forceinline__ void phase_sort(Frame& F0, int l) {
;     ...
;     lds_barrier();
;     { const int e = F.tid & 63, part = F.tid >> 6; int sa = 0, sb = 0;
;         for (int w = part * 32; w < part * 32 + 32; ++w) if (w < F.G) { const int h = HIST[w * 64 + e]; sa += h; if (w < F.vcu) sb += h; }
;         pa[part * 64 + e] = sa; pb[part * 64 + e] = sb; }
.LBB0_1409:
	s_or_b64 exec, exec, s[0:1]
	v_mov_b32_e32 v1, v200
	v_readlane_b32 s0, v252, 10
	v_readlane_b32 s4, v252, 4
	s_waitcnt lgkmcnt(0)
	s_barrier
	s_lshl_b32 s20, s0, 6
	s_mov_b64 s[14:15], 0
	v_readlane_b32 s6, v252, 6
	v_add_u32_e32 v0, s20, v1
	v_readlane_b32 s7, v252, 7
	s_add_u32 s22, s6, s14
	s_addc_u32 s23, s7, s15
	s_waitcnt lgkmcnt(0)
	s_barrier
	v_ashrrev_i32_e32 v3, 1, v0
	s_add_u32 s2, s22, 0xc00000
	v_and_b32_e32 v2, 63, v1
	v_and_b32_e32 v7, 0xffffffe0, v3
	v_or_b32_e32 v4, 31, v3
	v_lshlrev_b32_e32 v3, 6, v3
	s_movk_i32 s4, 0xf800
	s_mov_b64 s[0:1], 0
	s_addc_u32 s3, s23, 0
	v_and_or_b32 v2, v3, s4, v2
	v_mov_b32_e32 v5, 0
	v_mov_b32_e32 v6, 0
	v_readlane_b32 s5, v252, 5
	v_ashrrev_i32_e32 v3, 31, v2
	v_lshl_add_u64 v[8:9], v[2:3], 2, s[2:3]
	v_readlane_b32 s6, v254, 12
	s_mov_b64 s[8:9], 0x1000
	v_lshl_add_u64 v[10:11], v[8:9], 0, s[8:9]
	global_load_dword v100, v[8:9], off
	global_load_dword v101, v[8:9], off offset:256
	global_load_dword v102, v[8:9], off offset:512
	global_load_dword v103, v[8:9], off offset:768
	global_load_dword v104, v[8:9], off offset:1024
	global_load_dword v105, v[8:9], off offset:1280
	global_load_dword v106, v[8:9], off offset:1536
	global_load_dword v107, v[8:9], off offset:1792
	global_load_dword v108, v[8:9], off offset:2048
	global_load_dword v109, v[8:9], off offset:2304
	global_load_dword v110, v[8:9], off offset:2560
	global_load_dword v111, v[8:9], off offset:2816
	global_load_dword v112, v[8:9], off offset:3072
	global_load_dword v113, v[8:9], off offset:3328
	global_load_dword v114, v[8:9], off offset:3584
	global_load_dword v115, v[8:9], off offset:3840
	global_load_dword v116, v[10:11], off
	global_load_dword v117, v[10:11], off offset:256
	global_load_dword v118, v[10:11], off offset:512
	global_load_dword v119, v[10:11], off offset:768
	global_load_dword v120, v[10:11], off offset:1024
	global_load_dword v121, v[10:11], off offset:1280
	global_load_dword v122, v[10:11], off offset:1536
	global_load_dword v123, v[10:11], off offset:1792
	global_load_dword v124, v[10:11], off offset:2048
	global_load_dword v125, v[10:11], off offset:2304
	global_load_dword v126, v[10:11], off offset:2560
	global_load_dword v127, v[10:11], off offset:2816
	global_load_dword v128, v[10:11], off offset:3072
	global_load_dword v129, v[10:11], off offset:3328
	global_load_dword v130, v[10:11], off offset:3584
	global_load_dword v131, v[10:11], off offset:3840
	v_add_u32_e32 v3, 0, v7
	v_cmp_gt_i32_e64 s[8:9], s70, v3
	v_cmp_gt_i32_e64 s[12:13], s6, v3
	s_waitcnt vmcnt(31)
	s_nop 0
	v_cndmask_b32_e64 v12, 0, v100, s[8:9]
	v_cndmask_b32_e64 v13, 0, v12, s[12:13]
	v_add_u32_e32 v5, v12, v5
	v_add_u32_e32 v6, v13, v6
	v_add_u32_e32 v3, 1, v7
	v_cmp_gt_i32_e64 s[8:9], s70, v3
	v_cmp_gt_i32_e64 s[12:13], s6, v3
	s_waitcnt vmcnt(30)
	s_nop 0
	v_cndmask_b32_e64 v12, 0, v101, s[8:9]
	v_cndmask_b32_e64 v13, 0, v12, s[12:13]
	v_add_u32_e32 v5, v12, v5
	v_add_u32_e32 v6, v13, v6
	v_add_u32_e32 v3, 2, v7
	v_cmp_gt_i32_e64 s[8:9], s70, v3
	v_cmp_gt_i32_e64 s[12:13], s6, v3
	s_waitcnt vmcnt(29)
	s_nop 0
	v_cndmask_b32_e64 v12, 0, v102, s[8:9]
	v_cndmask_b32_e64 v13, 0, v12, s[12:13]
	v_add_u32_e32 v5, v12, v5
	v_add_u32_e32 v6, v13, v6
	v_add_u32_e32 v3, 3, v7
	v_cmp_gt_i32_e64 s[8:9], s70, v3
	v_cmp_gt_i32_e64 s[12:13], s6, v3
	s_waitcnt vmcnt(28)
	s_nop 0
	v_cndmask_b32_e64 v12, 0, v103, s[8:9]
	v_cndmask_b32_e64 v13, 0, v12, s[12:13]
	v_add_u32_e32 v5, v12, v5
	v_add_u32_e32 v6, v13, v6
	v_add_u32_e32 v3, 4, v7
	v_cmp_gt_i32_e64 s[8:9], s70, v3
	v_cmp_gt_i32_e64 s[12:13], s6, v3
	s_waitcnt vmcnt(27)
	s_nop 0
	v_cndmask_b32_e64 v12, 0, v104, s[8:9]
	v_cndmask_b32_e64 v13, 0, v12, s[12:13]
	v_add_u32_e32 v5, v12, v5
	v_add_u32_e32 v6, v13, v6
	v_add_u32_e32 v3, 5, v7
	v_cmp_gt_i32_e64 s[8:9], s70, v3
	v_cmp_gt_i32_e64 s[12:13], s6, v3
	s_waitcnt vmcnt(26)
	s_nop 0
	v_cndmask_b32_e64 v12, 0, v105, s[8:9]
	v_cndmask_b32_e64 v13, 0, v12, s[12:13]
	v_add_u32_e32 v5, v12, v5
	v_add_u32_e32 v6, v13, v6
	v_add_u32_e32 v3, 6, v7
	v_cmp_gt_i32_e64 s[8:9], s70, v3
	v_cmp_gt_i32_e64 s[12:13], s6, v3
	s_waitcnt vmcnt(25)
	s_nop 0
	v_cndmask_b32_e64 v12, 0, v106, s[8:9]
	v_cndmask_b32_e64 v13, 0, v12, s[12:13]
	v_add_u32_e32 v5, v12, v5
	v_add_u32_e32 v6, v13, v6
	v_add_u32_e32 v3, 7, v7
	v_cmp_gt_i32_e64 s[8:9], s70, v3
	v_cmp_gt_i32_e64 s[12:13], s6, v3
	s_waitcnt vmcnt(24)
	s_nop 0
	v_cndmask_b32_e64 v12, 0, v107, s[8:9]
	v_cndmask_b32_e64 v13, 0, v12, s[12:13]
	v_add_u32_e32 v5, v12, v5
	v_add_u32_e32 v6, v13, v6
	v_add_u32_e32 v3, 8, v7
	v_cmp_gt_i32_e64 s[8:9], s70, v3
	v_cmp_gt_i32_e64 s[12:13], s6, v3
	s_waitcnt vmcnt(23)
	s_nop 0
	v_cndmask_b32_e64 v12, 0, v108, s[8:9]
	v_cndmask_b32_e64 v13, 0, v12, s[12:13]
	v_add_u32_e32 v5, v12, v5
	v_add_u32_e32 v6, v13, v6
	v_add_u32_e32 v3, 9, v7
	v_cmp_gt_i32_e64 s[8:9], s70, v3
	v_cmp_gt_i32_e64 s[12:13], s6, v3
	s_waitcnt vmcnt(22)
	s_nop 0
	v_cndmask_b32_e64 v12, 0, v109, s[8:9]
	v_cndmask_b32_e64 v13, 0, v12, s[12:13]
	v_add_u32_e32 v5, v12, v5
	v_add_u32_e32 v6, v13, v6
	v_add_u32_e32 v3, 10, v7
	v_cmp_gt_i32_e64 s[8:9], s70, v3
	v_cmp_gt_i32_e64 s[12:13], s6, v3
	s_waitcnt vmcnt(21)
	s_nop 0
	v_cndmask_b32_e64 v12, 0, v110, s[8:9]
	v_cndmask_b32_e64 v13, 0, v12, s[12:13]
	v_add_u32_e32 v5, v12, v5
	v_add_u32_e32 v6, v13, v6
	v_add_u32_e32 v3, 11, v7
	v_cmp_gt_i32_e64 s[8:9], s70, v3
	v_cmp_gt_i32_e64 s[12:13], s6, v3
	s_waitcnt vmcnt(20)
; __device__ __forceinline__ void phase_sort(Frame& F0, int l) {
;     ...
;     { const int e = F.tid & 63, part = F.tid >> 6; int sa = 0, sb = 0;
;         for (int w = part * 32; w < part * 32 + 32; ++w) if (w < F.G) { const int h = HIST[w * 64 + e]; sa += h; if (w < F.vcu) sb += h; }
;         pa[part * 64 + e] = sa; pb[part * 64 + e] = sb; }
	s_nop 0
	v_cndmask_b32_e64 v12, 0, v111, s[8:9]
	v_cndmask_b32_e64 v13, 0, v12, s[12:13]
	v_add_u32_e32 v5, v12, v5
	v_add_u32_e32 v6, v13, v6
	v_add_u32_e32 v3, 12, v7
	v_cmp_gt_i32_e64 s[8:9], s70, v3
	v_cmp_gt_i32_e64 s[12:13], s6, v3
	s_waitcnt vmcnt(19)
	s_nop 0
	v_cndmask_b32_e64 v12, 0, v112, s[8:9]
	v_cndmask_b32_e64 v13, 0, v12, s[12:13]
	v_add_u32_e32 v5, v12, v5
	v_add_u32_e32 v6, v13, v6
	v_add_u32_e32 v3, 13, v7
	v_cmp_gt_i32_e64 s[8:9], s70, v3
	v_cmp_gt_i32_e64 s[12:13], s6, v3
	s_waitcnt vmcnt(18)
	s_nop 0
	v_cndmask_b32_e64 v12, 0, v113, s[8:9]
	v_cndmask_b32_e64 v13, 0, v12, s[12:13]
	v_add_u32_e32 v5, v12, v5
	v_add_u32_e32 v6, v13, v6
	v_add_u32_e32 v3, 14, v7
	v_cmp_gt_i32_e64 s[8:9], s70, v3
	v_cmp_gt_i32_e64 s[12:13], s6, v3
	s_waitcnt vmcnt(17)
	s_nop 0
	v_cndmask_b32_e64 v12, 0, v114, s[8:9]
	v_cndmask_b32_e64 v13, 0, v12, s[12:13]
	v_add_u32_e32 v5, v12, v5
	v_add_u32_e32 v6, v13, v6
	v_add_u32_e32 v3, 15, v7
	v_cmp_gt_i32_e64 s[8:9], s70, v3
	v_cmp_gt_i32_e64 s[12:13], s6, v3
	s_waitcnt vmcnt(16)
	s_nop 0
	v_cndmask_b32_e64 v12, 0, v115, s[8:9]
	v_cndmask_b32_e64 v13, 0, v12, s[12:13]
	v_add_u32_e32 v5, v12, v5
	v_add_u32_e32 v6, v13, v6
	v_add_u32_e32 v3, 16, v7
	v_cmp_gt_i32_e64 s[8:9], s70, v3
	v_cmp_gt_i32_e64 s[12:13], s6, v3
	s_waitcnt vmcnt(15)
	s_nop 0
	v_cndmask_b32_e64 v12, 0, v116, s[8:9]
	v_cndmask_b32_e64 v13, 0, v12, s[12:13]
	v_add_u32_e32 v5, v12, v5
	v_add_u32_e32 v6, v13, v6
	v_add_u32_e32 v3, 17, v7
	v_cmp_gt_i32_e64 s[8:9], s70, v3
	v_cmp_gt_i32_e64 s[12:13], s6, v3
	s_waitcnt vmcnt(14)
	s_nop 0
	v_cndmask_b32_e64 v12, 0, v117, s[8:9]
	v_cndmask_b32_e64 v13, 0, v12, s[12:13]
	v_add_u32_e32 v5, v12, v5
	v_add_u32_e32 v6, v13, v6
	v_add_u32_e32 v3, 18, v7
	v_cmp_gt_i32_e64 s[8:9], s70, v3
	v_cmp_gt_i32_e64 s[12:13], s6, v3
	s_waitcnt vmcnt(13)
	s_nop 0
	v_cndmask_b32_e64 v12, 0, v118, s[8:9]
	v_cndmask_b32_e64 v13, 0, v12, s[12:13]
	v_add_u32_e32 v5, v12, v5
	v_add_u32_e32 v6, v13, v6
	v_add_u32_e32 v3, 19, v7
	v_cmp_gt_i32_e64 s[8:9], s70, v3
	v_cmp_gt_i32_e64 s[12:13], s6, v3
	s_waitcnt vmcnt(12)
	s_nop 0
	v_cndmask_b32_e64 v12, 0, v119, s[8:9]
	v_cndmask_b32_e64 v13, 0, v12, s[12:13]
	v_add_u32_e32 v5, v12, v5
	v_add_u32_e32 v6, v13, v6
	v_add_u32_e32 v3, 20, v7
	v_cmp_gt_i32_e64 s[8:9], s70, v3
	v_cmp_gt_i32_e64 s[12:13], s6, v3
	s_waitcnt vmcnt(11)
	s_nop 0
	v_cndmask_b32_e64 v12, 0, v120, s[8:9]
	v_cndmask_b32_e64 v13, 0, v12, s[12:13]
	v_add_u32_e32 v5, v12, v5
	v_add_u32_e32 v6, v13, v6
	v_add_u32_e32 v3, 21, v7
	v_cmp_gt_i32_e64 s[8:9], s70, v3
	v_cmp_gt_i32_e64 s[12:13], s6, v3
	s_waitcnt vmcnt(10)
	s_nop 0
	v_cndmask_b32_e64 v12, 0, v121, s[8:9]
	v_cndmask_b32_e64 v13, 0, v12, s[12:13]
	v_add_u32_e32 v5, v12, v5
	v_add_u32_e32 v6, v13, v6
	v_add_u32_e32 v3, 22, v7
	v_cmp_gt_i32_e64 s[8:9], s70, v3
	v_cmp_gt_i32_e64 s[12:13], s6, v3
	s_waitcnt vmcnt(9)
	s_nop 0
	v_cndmask_b32_e64 v12, 0, v122, s[8:9]
	v_cndmask_b32_e64 v13, 0, v12, s[12:13]
	v_add_u32_e32 v5, v12, v5
	v_add_u32_e32 v6, v13, v6
	v_add_u32_e32 v3, 23, v7
	v_cmp_gt_i32_e64 s[8:9], s70, v3
	v_cmp_gt_i32_e64 s[12:13], s6, v3
	s_waitcnt vmcnt(8)
	s_nop 0
	v_cndmask_b32_e64 v12, 0, v123, s[8:9]
	v_cndmask_b32_e64 v13, 0, v12, s[12:13]
	v_add_u32_e32 v5, v12, v5
	v_add_u32_e32 v6, v13, v6
	v_add_u32_e32 v3, 24, v7
	v_cmp_gt_i32_e64 s[8:9], s70, v3
	v_cmp_gt_i32_e64 s[12:13], s6, v3
	s_waitcnt vmcnt(7)
	s_nop 0
	v_cndmask_b32_e64 v12, 0, v124, s[8:9]
	v_cndmask_b32_e64 v13, 0, v12, s[12:13]
	v_add_u32_e32 v5, v12, v5
	v_add_u32_e32 v6, v13, v6
	v_add_u32_e32 v3, 25, v7
	v_cmp_gt_i32_e64 s[8:9], s70, v3
	v_cmp_gt_i32_e64 s[12:13], s6, v3
	s_waitcnt vmcnt(6)
	s_nop 0
	v_cndmask_b32_e64 v12, 0, v125, s[8:9]
	v_cndmask_b32_e64 v13, 0, v12, s[12:13]
	v_add_u32_e32 v5, v12, v5
	v_add_u32_e32 v6, v13, v6
	v_add_u32_e32 v3, 26, v7
	v_cmp_gt_i32_e64 s[8:9], s70, v3
	v_cmp_gt_i32_e64 s[12:13], s6, v3
	s_waitcnt vmcnt(5)
	s_nop 0
	v_cndmask_b32_e64 v12, 0, v126, s[8:9]
	v_cndmask_b32_e64 v13, 0, v12, s[12:13]
	v_add_u32_e32 v5, v12, v5
	v_add_u32_e32 v6, v13, v6
	v_add_u32_e32 v3, 27, v7
	v_cmp_gt_i32_e64 s[8:9], s70, v3
	v_cmp_gt_i32_e64 s[12:13], s6, v3
	s_waitcnt vmcnt(4)
	s_nop 0
	v_cndmask_b32_e64 v12, 0, v127, s[8:9]
	v_cndmask_b32_e64 v13, 0, v12, s[12:13]
	v_add_u32_e32 v5, v12, v5
	v_add_u32_e32 v6, v13, v6
	v_add_u32_e32 v3, 28, v7
	v_cmp_gt_i32_e64 s[8:9], s70, v3
	v_cmp_gt_i32_e64 s[12:13], s6, v3
	s_waitcnt vmcnt(3)
	s_nop 0
	v_cndmask_b32_e64 v12, 0, v128, s[8:9]
	v_cndmask_b32_e64 v13, 0, v12, s[12:13]
	v_add_u32_e32 v5, v12, v5
	v_add_u32_e32 v6, v13, v6
	v_add_u32_e32 v3, 29, v7
	v_cmp_gt_i32_e64 s[8:9], s70, v3
	v_cmp_gt_i32_e64 s[12:13], s6, v3
	s_waitcnt vmcnt(2)
	s_nop 0
	v_cndmask_b32_e64 v12, 0, v129, s[8:9]
	v_cndmask_b32_e64 v13, 0, v12, s[12:13]
	v_add_u32_e32 v5, v12, v5
	v_add_u32_e32 v6, v13, v6
	v_add_u32_e32 v3, 30, v7
	v_cmp_gt_i32_e64 s[8:9], s70, v3
	v_cmp_gt_i32_e64 s[12:13], s6, v3
	s_waitcnt vmcnt(1)
	s_nop 0
	v_cndmask_b32_e64 v12, 0, v130, s[8:9]
	v_cndmask_b32_e64 v13, 0, v12, s[12:13]
	v_add_u32_e32 v5, v12, v5
	v_add_u32_e32 v6, v13, v6
	v_add_u32_e32 v3, 31, v7
	v_cmp_gt_i32_e64 s[8:9], s70, v3
	v_cmp_gt_i32_e64 s[12:13], s6, v3
	s_waitcnt vmcnt(0)
	s_nop 0
	v_cndmask_b32_e64 v12, 0, v131, s[8:9]
	v_cndmask_b32_e64 v13, 0, v12, s[12:13]
	v_add_u32_e32 v5, v12, v5
	v_add_u32_e32 v6, v13, v6

; template <class Sched> __device__ __forceinline__ unsigned gather_off(const Sched& S, int ui, int h, int i, int t, int KB) { asm volatile("" : "+v"(t)); int R, C; stage_rc(t * 16 + i * 8192, R, C); return (unsigned)(S.arow(ui, h * HALF + R) * KB + C * 2); }
; #define PG8_BAR __builtin_amdgcn_s_barrier()
;     ...
;     PG8_STAGE(PG8_SB(0, 0), cB, voffB); PG8_STAGE(PG8_SB(0, 1), cB + hstep, voffB); PG8_STAGE_A(PG8_SA(0, 0), cA, oc, 0); PG8_STAGE_A(PG8_SA(0, 1), cA, oc, 1);
;     if (wr == 1) PG8_BAR;
;     PG8_WAIT_V(2); PG8_BAR;
;     PG8_STAGE(PG8_SB(1, 0), cB + kstep, voffB); PG8_STAGE_A(PG8_SA(1, 0), cA + kstep, oc, 0); PG8_STAGE(PG8_SB(1, 1), cB + hstep + kstep, voffB);
;     PG8_WAIT_V(6); PG8_BAR;
;     for (;;) {
;         const bool has_next = S.next(ui + 1, nxt);
;         const char* nA = cA; const char* nB = has_next ? uptr((const char*)g.Bt + (size_t)nxt.e * g.bstride + (size_t)nxt.pn * tstep) : cB;
;         if constexpr (GATHER) {
;         } else { if (has_next) nA = uptr((const char*)g.A + (size_t)nxt.pm * tstep); }
; #pragma unroll 1
;         for (int t = 0; t < nt; t += 2) {
;             const bool last = (t == nt - 2);
;             const char* a1 = cA + (size_t)(t + 1) * kstep;
;             const char* a2 = last ? nA : cA + (size_t)(t + 2) * kstep; const char* b2 = last ? nB : cB + (size_t)(t + 2) * kstep;
;             const char* a3 = a2 + kstep; const char* b3 = b2 + kstep;
;             unsigned o2[2][2];
; #pragma unroll
;             for (int h = 0; h < 2; ++h)
; #pragma unroll
;                 for (int i = 0; i < 2; ++i) o2[h][i] = oc[h][i];
;             if constexpr (GATHER) { if (last && has_next) {
; #pragma unroll
;                 for (int h = 0; h < 2; ++h)
; #pragma unroll
;                     for (int i = 0; i < 2; ++i) o2[h][i] = gather_off(S, ui + 1, h, i, tid, KB); } }
;             if (last && has_next) S.a_ready(nxt);
;             PG8_LDB(B0, 0, 0); PG8_LDB(B1, 0, 1); PG8_SCHED; PG8_LDA(At, 0, 0); PG8_STAGE_A(PG8_SA(1, 1), a1, oc, 1);
;             PG8_WAIT_V(8); PG8_WAIT_L(0); PG8_BAR; PG8_MMA(0, 0, At, B0); PG8_MMA(0, 1, At, B1); PG8_BAR; PG8_SCHED;
;             PG8_LDA(At, 0, 1); PG8_STAGE(PG8_SB(0, 0), b2, voffB); PG8_STAGE(PG8_SB(0, 1), b2 + hstep, voffB); PG8_STAGE_A(PG8_SA(0, 0), a2, o2, 0);
;             PG8_WAIT_V(8); PG8_WAIT_L(0); PG8_BAR; PG8_MMA(1, 0, At, B0); PG8_MMA(1, 1, At, B1); PG8_BAR; PG8_SCHED;
.LBB0_1630:
	s_add_i32 s17, s2, 0
	s_and_b32 s41, s3, 0xffff
	s_lshl_b32 s3, s5, 5
	s_add_i32 s18, s17, 0x18000
	s_and_b32 s16, s3, 0x60
	v_lshl_add_u64 v[0:1], v[0:1], 0, s[92:93]
	s_mov_b32 m0, s18
	s_add_i32 s19, s17, 0x1a000
	s_lshr_b32 s14, s16, 3
	s_waitcnt vmcnt(2)
	s_barrier
	global_load_lds_dwordx4 v[0:1], off
	v_lshl_add_u64 v[0:1], v[2:3], 0, s[92:93]
	s_mov_b32 m0, s19
	s_add_i32 s28, s17, 0x8000
	s_add_i32 s29, s17, 0xa000
	global_load_lds_dwordx4 v[0:1], off
	v_lshl_add_u64 v[0:1], v[4:5], 0, s[92:93]
	s_mov_b32 m0, s28
	s_add_u32 s2, s20, 0x8080
	global_load_lds_dwordx4 v[0:1], off
	v_lshl_add_u64 v[0:1], v[6:7], 0, s[92:93]
	s_mov_b32 m0, s29
	s_addc_u32 s3, s21, 0
	s_add_i32 s38, s17, 0x1c000
	global_load_lds_dwordx4 v[0:1], off
	v_lshl_add_u64 v[0:1], s[2:3], 0, v[180:181]
	s_mov_b32 m0, s38
	s_add_i32 s39, s17, 0x1e000
	global_load_lds_dwordx4 v[0:1], off
	v_lshl_add_u64 v[0:1], s[2:3], 0, v[132:133]
	s_mov_b32 m0, s39
	v_lshlrev_b32_e32 v3, 1, v8
	global_load_lds_dwordx4 v[0:1], off
	v_and_b32_e32 v0, 15, v8
	v_lshlrev_b32_e32 v1, 2, v8
	v_and_b32_e32 v3, 32, v3
	v_and_b32_e32 v1, 32, v1
	v_bfe_u32 v2, v8, 5, 1
	v_lshl_or_b32 v0, v0, 6, v3
	v_or_b32_e32 v4, s14, v2
	s_waitcnt vmcnt(0)
	v_xad_u32 v0, v0, v1, 0
	v_lshlrev_b32_e32 v3, 13, v9
	v_lshl_add_u32 v1, v4, 10, v0
	v_lshl_add_u32 v0, v2, 10, v0
	v_mov_b32_e32 v137, v181
	v_mov_b32_e32 v131, v181
	v_lshlrev_b32_e32 v140, 6, v9
	s_mov_b32 s40, 1
	v_add_u32_e32 v141, 0x10000, v1
	v_add_u32_e32 v142, 0x10010, v1
	v_add_u32_e32 v143, 0x14000, v1
	v_add_u32_e32 v144, 0x14010, v1
	v_add_u32_e32 v145, 0x18000, v1
	v_add_u32_e32 v146, 0x18010, v1
	v_add_u32_e32 v147, 0x1c000, v1
	v_add_u32_e32 v148, 0x1c010, v1
	v_add_u32_e32 v149, 0x10800, v1
	v_add_u32_e32 v150, 0x10810, v1
	v_add_u32_e32 v151, 0x14800, v1
	v_add_u32_e32 v152, 0x14810, v1
	v_add_u32_e32 v153, 0x18800, v1
	v_add_u32_e32 v154, 0x18810, v1
	v_add_u32_e32 v155, 0x1c800, v1
	v_add_u32_e32 v156, 0x1c810, v1
	s_mov_b32 s42, 0
	v_add_u32_e32 v157, v0, v3
	s_barrier
	s_branch .LBB0_1632
.LBB0_1631:
	ds_read_b128 v[24:27], v141
	ds_read_b128 v[28:31], v142
	ds_read_b128 v[56:59], v149
	ds_read_b128 v[60:63], v150
	ds_read_b128 v[158:161], v143
	ds_read_b128 v[162:165], v144
	ds_read_b128 v[166:169], v151
	ds_read_b128 v[170:173], v152
	s_add_u32 s2, s20, 0x8000
	s_addc_u32 s3, s21, 0
	v_lshl_add_u64 v[0:1], s[0:1], 0, v[136:137]
	v_lshl_add_u64 v[0:1], v[0:1], 0, s[92:93]
	s_add_i32 m0, s17, 0xc000
	ds_read_b128 v[4:7], v157
	ds_read_b128 v[8:11], v157 offset:16
	ds_read_b128 v[12:15], v157 offset:2048
	ds_read_b128 v[16:19], v157 offset:2064
	ds_read_b128 v[40:43], v157 offset:4096
	ds_read_b128 v[44:47], v157 offset:4112
	ds_read_b128 v[72:75], v157 offset:6144
	ds_read_b128 v[76:79], v157 offset:6160
	global_load_lds_dwordx4 v[0:1], off
	v_lshl_add_u64 v[0:1], s[0:1], 0, v[130:131]
	v_lshl_add_u64 v[0:1], v[0:1], 0, s[92:93]
	s_add_i32 m0, s17, 0xe000
	s_nop 0
	global_load_lds_dwordx4 v[0:1], off
	s_waitcnt vmcnt(16)
	s_waitcnt lgkmcnt(0)
	s_barrier
	s_setprio 1
	s_waitcnt lgkmcnt(0)
	v_mfma_scale_f32_16x16x128_f8f6f4 v[116:119], v[24:31], v[4:11], 0, v211, v212 op_sel_hi:[0,0,0]
	v_mfma_scale_f32_16x16x128_f8f6f4 v[112:115], v[56:63], v[4:11], 0, v211, v212 op_sel_hi:[0,0,0]
	v_mfma_scale_f32_16x16x128_f8f6f4 v[100:103], v[24:31], v[12:19], 0, v211, v212 op_sel_hi:[0,0,0]
	v_mfma_scale_f32_16x16x128_f8f6f4 v[96:99], v[56:63], v[12:19], 0, v211, v212 op_sel_hi:[0,0,0]
	v_mfma_scale_f32_16x16x128_f8f6f4 v[68:71], v[24:31], v[40:47], 0, v211, v212 op_sel_hi:[0,0,0]
	v_mfma_scale_f32_16x16x128_f8f6f4 v[64:67], v[56:63], v[40:47], 0, v211, v212 op_sel_hi:[0,0,0]
	v_mfma_scale_f32_16x16x128_f8f6f4 v[36:39], v[24:31], v[72:79], 0, v211, v212 op_sel_hi:[0,0,0]
	v_mfma_scale_f32_16x16x128_f8f6f4 v[32:35], v[56:63], v[72:79], 0, v211, v212 op_sel_hi:[0,0,0]
	s_setprio 0
	s_setprio 1
	v_mfma_scale_f32_16x16x128_f8f6f4 v[124:127], v[158:165], v[4:11], 0, v211, v212 op_sel_hi:[0,0,0]
	v_mfma_scale_f32_16x16x128_f8f6f4 v[120:123], v[166:173], v[4:11], 0, v211, v212 op_sel_hi:[0,0,0]
	v_mfma_scale_f32_16x16x128_f8f6f4 v[108:111], v[158:165], v[12:19], 0, v211, v212 op_sel_hi:[0,0,0]
	v_mfma_scale_f32_16x16x128_f8f6f4 v[104:107], v[166:173], v[12:19], 0, v211, v212 op_sel_hi:[0,0,0]
	v_mfma_scale_f32_16x16x128_f8f6f4 v[84:87], v[158:165], v[40:47], 0, v211, v212 op_sel_hi:[0,0,0]
	v_mfma_scale_f32_16x16x128_f8f6f4 v[80:83], v[166:173], v[40:47], 0, v211, v212 op_sel_hi:[0,0,0]
	v_mfma_scale_f32_16x16x128_f8f6f4 v[52:55], v[158:165], v[72:79], 0, v211, v212 op_sel_hi:[0,0,0]
	v_mfma_scale_f32_16x16x128_f8f6f4 v[48:51], v[166:173], v[72:79], 0, v211, v212 op_sel_hi:[0,0,0]
	s_setprio 0
	s_barrier
	v_lshl_add_u64 v[138:139], s[20:21], 0, v[180:181]
	s_add_i32 m0, s17, 0x10000
	ds_read_b128 v[182:185], v157 offset:16384
	ds_read_b128 v[186:189], v157 offset:16400
	ds_read_b128 v[190:193], v157 offset:18432
	ds_read_b128 v[194:197], v157 offset:18448
	ds_read_b128 v[202:205], v157 offset:20480
	ds_read_b128 v[206:209], v157 offset:20496
	ds_read_b128 v[220:223], v157 offset:22528
	ds_read_b128 v[224:227], v157 offset:22544
	global_load_lds_dwordx4 v[138:139], off
	v_lshl_add_u64 v[174:175], s[20:21], 0, v[132:133]
	s_add_i32 m0, s17, 0x12000
	v_lshl_add_u64 v[4:5], s[2:3], 0, v[180:181]
	global_load_lds_dwordx4 v[174:175], off
	s_add_i32 m0, s17, 0x14000
	v_lshl_add_u64 v[176:177], s[36:37], 0, v[134:135]
	global_load_lds_dwordx4 v[4:5], off
	v_lshl_add_u64 v[4:5], s[2:3], 0, v[132:133]
	s_add_i32 m0, s17, 0x16000
	v_lshl_add_u64 v[178:179], s[36:37], 0, v[128:129]
	global_load_lds_dwordx4 v[4:5], off
	s_mov_b32 m0, s17
	s_nop 0
	global_load_lds_dwordx4 v[176:177], off
	s_add_i32 m0, s17, 0x2000
	s_nop 0
	global_load_lds_dwordx4 v[178:179], off
	s_waitcnt vmcnt(16)
	s_waitcnt lgkmcnt(0)
	s_barrier
; #define PG8_STAGE(bufoff, gbase, voff) do { _Pragma("unroll") for (int _i = 0; _i < 2; ++_i) \
;         __builtin_amdgcn_global_load_lds((const unsigned*)((const char*)(gbase) + (voff)[_i]), (PG8_LAS unsigned*)(lds + (bufoff) + ldsw + _i * 8192), 16, 0, 0); } while (0)
; #define PG8_STAGE_A(bufoff, gbase, OA, h) do { _Pragma("unroll") for (int _i = 0; _i < 2; ++_i) \
;         __builtin_amdgcn_global_load_lds((const unsigned*)((const char*)(gbase) + (OA)[h][_i]), (PG8_LAS unsigned*)(lds + (bufoff) + ldsw + _i * 8192), 16, 0, 0); } while (0)
; #define PG8_WAIT_V(n) asm volatile("s_waitcnt vmcnt(" #n ")" ::: "memory")
; #define PG8_WAIT_L(n) asm volatile("s_waitcnt lgkmcnt(" #n ")" ::: "memory")
; #define PG8_BAR __builtin_amdgcn_s_barrier()
; #define PG8_SCHED __builtin_amdgcn_sched_barrier(0)
;     ...
;             PG8_WAIT_V(8); PG8_WAIT_L(0); PG8_BAR; PG8_MMA(1, 0, At, B0); PG8_MMA(1, 1, At, B1); PG8_BAR; PG8_SCHED;
;             PG8_LDB(B0, 1, 0); PG8_LDB(B1, 1, 1); PG8_SCHED; PG8_LDA(At, 1, 0); PG8_STAGE_A(PG8_SA(0, 1), a2, o2, 1);
;             PG8_WAIT_V(8); PG8_WAIT_L(0); PG8_BAR; PG8_MMA(0, 0, At, B0); PG8_MMA(0, 1, At, B1); PG8_BAR; PG8_SCHED;
;             PG8_LDA(At, 1, 1); PG8_STAGE(PG8_SB(1, 0), b3, voffB); PG8_STAGE(PG8_SB(1, 1), b3 + hstep, voffB); PG8_STAGE_A(PG8_SA(1, 0), a3, o2, 0);
;             PG8_WAIT_V(8); PG8_WAIT_L(0); PG8_BAR; PG8_MMA(1, 0, At, B0); PG8_MMA(1, 1, At, B1); PG8_BAR; PG8_SCHED;
	s_setprio 1
	s_waitcnt lgkmcnt(0)
	v_mfma_scale_f32_16x16x128_f8f6f4 v[76:79], v[24:31], v[182:189], 0, v211, v212 op_sel_hi:[0,0,0]
	v_mfma_scale_f32_16x16x128_f8f6f4 v[72:75], v[56:63], v[182:189], 0, v211, v212 op_sel_hi:[0,0,0]
	v_mfma_scale_f32_16x16x128_f8f6f4 v[44:47], v[24:31], v[190:197], 0, v211, v212 op_sel_hi:[0,0,0]
	v_mfma_scale_f32_16x16x128_f8f6f4 v[40:43], v[56:63], v[190:197], 0, v211, v212 op_sel_hi:[0,0,0]
	v_mfma_scale_f32_16x16x128_f8f6f4 v[20:23], v[24:31], v[202:209], 0, v211, v212 op_sel_hi:[0,0,0]
	v_mfma_scale_f32_16x16x128_f8f6f4 v[16:19], v[56:63], v[202:209], 0, v211, v212 op_sel_hi:[0,0,0]
	v_mfma_scale_f32_16x16x128_f8f6f4 v[8:11], v[24:31], v[220:227], 0, v211, v212 op_sel_hi:[0,0,0]
	v_mfma_scale_f32_16x16x128_f8f6f4 v[4:7], v[56:63], v[220:227], 0, v211, v212 op_sel_hi:[0,0,0]
	s_setprio 0
	s_setprio 1
	v_mfma_scale_f32_16x16x128_f8f6f4 v[92:95], v[158:165], v[182:189], 0, v211, v212 op_sel_hi:[0,0,0]
	v_mfma_scale_f32_16x16x128_f8f6f4 v[88:91], v[166:173], v[182:189], 0, v211, v212 op_sel_hi:[0,0,0]
	v_mfma_scale_f32_16x16x128_f8f6f4 v[60:63], v[158:165], v[190:197], 0, v211, v212 op_sel_hi:[0,0,0]
	v_mfma_scale_f32_16x16x128_f8f6f4 v[56:59], v[166:173], v[190:197], 0, v211, v212 op_sel_hi:[0,0,0]
	v_mfma_scale_f32_16x16x128_f8f6f4 v[28:31], v[158:165], v[202:209], 0, v211, v212 op_sel_hi:[0,0,0]
	v_mfma_scale_f32_16x16x128_f8f6f4 v[24:27], v[166:173], v[202:209], 0, v211, v212 op_sel_hi:[0,0,0]
	v_mfma_scale_f32_16x16x128_f8f6f4 v[12:15], v[158:165], v[220:227], 0, v211, v212 op_sel_hi:[0,0,0]
	v_mfma_scale_f32_16x16x128_f8f6f4 v[0:3], v[166:173], v[220:227], 0, v211, v212 op_sel_hi:[0,0,0]
	s_setprio 0
	s_barrier
	ds_read_b128 v[158:161], v145
	ds_read_b128 v[162:165], v146
	ds_read_b128 v[166:169], v153
	ds_read_b128 v[170:173], v154
	ds_read_b128 v[182:185], v147
	ds_read_b128 v[186:189], v148
	ds_read_b128 v[190:193], v155
	ds_read_b128 v[194:197], v156
	v_lshl_add_u64 v[198:199], s[36:37], 0, v[136:137]
	s_add_i32 m0, s17, 0x4000
	ds_read_b128 v[202:205], v157 offset:32768
	ds_read_b128 v[206:209], v157 offset:32784
	ds_read_b128 v[220:223], v157 offset:34816
	ds_read_b128 v[224:227], v157 offset:34832
	ds_read_b128 v[236:239], v157 offset:36864
	ds_read_b128 v[240:243], v157 offset:36880
	ds_read_b128 v[244:247], v157 offset:38912
	ds_read_b128 v[248:251], v157 offset:38928
	global_load_lds_dwordx4 v[198:199], off
	v_lshl_add_u64 v[198:199], s[36:37], 0, v[130:131]
	s_add_i32 m0, s17, 0x6000
	s_nop 0
	global_load_lds_dwordx4 v[198:199], off
	s_waitcnt vmcnt(8)
	s_waitcnt lgkmcnt(0)
	s_barrier
	s_setprio 1
	s_waitcnt lgkmcnt(0)
	v_mfma_scale_f32_16x16x128_f8f6f4 v[116:119], v[158:165], v[202:209], v[116:119], v211, v212 op_sel_hi:[0,0,0]
	v_mfma_scale_f32_16x16x128_f8f6f4 v[112:115], v[166:173], v[202:209], v[112:115], v211, v212 op_sel_hi:[0,0,0]
	v_mfma_scale_f32_16x16x128_f8f6f4 v[100:103], v[158:165], v[220:227], v[100:103], v211, v212 op_sel_hi:[0,0,0]
	v_mfma_scale_f32_16x16x128_f8f6f4 v[96:99], v[166:173], v[220:227], v[96:99], v211, v212 op_sel_hi:[0,0,0]
	v_mfma_scale_f32_16x16x128_f8f6f4 v[68:71], v[158:165], v[236:243], v[68:71], v211, v212 op_sel_hi:[0,0,0]
	v_mfma_scale_f32_16x16x128_f8f6f4 v[64:67], v[166:173], v[236:243], v[64:67], v211, v212 op_sel_hi:[0,0,0]
	v_mfma_scale_f32_16x16x128_f8f6f4 v[36:39], v[158:165], v[244:251], v[36:39], v211, v212 op_sel_hi:[0,0,0]
	v_mfma_scale_f32_16x16x128_f8f6f4 v[32:35], v[166:173], v[244:251], v[32:35], v211, v212 op_sel_hi:[0,0,0]
	s_setprio 0
	s_setprio 1
	v_mfma_scale_f32_16x16x128_f8f6f4 v[124:127], v[182:189], v[202:209], v[124:127], v211, v212 op_sel_hi:[0,0,0]
	v_mfma_scale_f32_16x16x128_f8f6f4 v[120:123], v[190:197], v[202:209], v[120:123], v211, v212 op_sel_hi:[0,0,0]
	v_mfma_scale_f32_16x16x128_f8f6f4 v[108:111], v[182:189], v[220:227], v[108:111], v211, v212 op_sel_hi:[0,0,0]
	v_mfma_scale_f32_16x16x128_f8f6f4 v[104:107], v[190:197], v[220:227], v[104:107], v211, v212 op_sel_hi:[0,0,0]
	v_mfma_scale_f32_16x16x128_f8f6f4 v[84:87], v[182:189], v[236:243], v[84:87], v211, v212 op_sel_hi:[0,0,0]
	v_mfma_scale_f32_16x16x128_f8f6f4 v[80:83], v[190:197], v[236:243], v[80:83], v211, v212 op_sel_hi:[0,0,0]
	v_mfma_scale_f32_16x16x128_f8f6f4 v[52:55], v[182:189], v[244:251], v[52:55], v211, v212 op_sel_hi:[0,0,0]
	v_mfma_scale_f32_16x16x128_f8f6f4 v[48:51], v[190:197], v[244:251], v[48:51], v211, v212 op_sel_hi:[0,0,0]
	s_setprio 0
	s_barrier
	s_mov_b32 m0, s18
	v_lshl_add_u64 v[138:139], v[138:139], 0, s[92:93]
	s_add_u32 s0, s20, 0x8080
	ds_read_b128 v[202:205], v157 offset:49152
	ds_read_b128 v[206:209], v157 offset:49168
	ds_read_b128 v[220:223], v157 offset:51200
	ds_read_b128 v[224:227], v157 offset:51216
	ds_read_b128 v[236:239], v157 offset:53248
	ds_read_b128 v[240:243], v157 offset:53264
	ds_read_b128 v[244:247], v157 offset:55296
	ds_read_b128 v[248:251], v157 offset:55312
	global_load_lds_dwordx4 v[138:139], off
	v_lshl_add_u64 v[138:139], v[174:175], 0, s[92:93]
	s_mov_b32 m0, s19
	s_addc_u32 s1, s21, 0
	global_load_lds_dwordx4 v[138:139], off
	v_lshl_add_u64 v[138:139], s[0:1], 0, v[180:181]
	s_mov_b32 m0, s38
	s_nop 0
	global_load_lds_dwordx4 v[138:139], off
	v_lshl_add_u64 v[138:139], s[0:1], 0, v[132:133]
	s_mov_b32 m0, s39
	s_nop 0
	global_load_lds_dwordx4 v[138:139], off
	v_lshl_add_u64 v[138:139], v[176:177], 0, s[92:93]
	s_mov_b32 m0, s28
	s_nop 0
	global_load_lds_dwordx4 v[138:139], off
	v_lshl_add_u64 v[138:139], v[178:179], 0, s[92:93]
	s_mov_b32 m0, s29
	s_nop 0
	global_load_lds_dwordx4 v[138:139], off
	s_waitcnt vmcnt(8)
	s_waitcnt lgkmcnt(0)
	s_barrier
; __device__ __forceinline__ unsigned pk4f8(float a, float b, float c, float d) { int w = 0; w = __builtin_amdgcn_cvt_pk_fp8_f32(a, b, w, false); w = __builtin_amdgcn_cvt_pk_fp8_f32(c, d, w, true); return (unsigned)w; }
; #define PG8_STAGE(bufoff, gbase, voff) do { _Pragma("unroll") for (int _i = 0; _i < 2; ++_i) \
;         __builtin_amdgcn_global_load_lds((const unsigned*)((const char*)(gbase) + (voff)[_i]), (PG8_LAS unsigned*)(lds + (bufoff) + ldsw + _i * 8192), 16, 0, 0); } while (0)
; #define PG8_WAIT_V(n) asm volatile("s_waitcnt vmcnt(" #n ")" ::: "memory")
; #define PG8_WAIT_L(n) asm volatile("s_waitcnt lgkmcnt(" #n ")" ::: "memory")
; #define PG8_BAR __builtin_amdgcn_s_barrier()
; #define PG8_SCHED __builtin_amdgcn_sched_barrier(0)
;     __device__ __forceinline__ void operator()(const f32x4 (&acc)[2][2][4][2], const Unit& u, int wr, int wc, int fr, int fq) const {
;         unsigned char* base = O; int pm = u.pm; int ld = ldc; if (pm >= pm_split) { base = O2; pm -= pm_off2; ld = ldc2; }
;         const int row0 = pm * BM + wr * 64 + fr; const int col0 = u.pn * BM + wc * 32 + ((fq & 1) ? HALF + 8 * (fq - 1) : 8 * fq);
; #pragma unroll
;         for (int ai = 0; ai < 2; ++ai)
; #pragma unroll
;             for (int m = 0; m < 4; ++m) { unsigned char* rowp = base + (size_t)(row0 + ai * HALF + m * 16) * ld + col0;
;                 const f32x4 p0 = acc[ai][0][m][0] * scale, p1 = acc[ai][0][m][1] * scale, q0 = acc[ai][1][m][0] * scale, q1 = acc[ai][1][m][1] * scale;
;                 unsigned ax = pk4f8(p0[0], p0[1], p0[2], p0[3]), ay = pk4f8(p1[0], p1[1], p1[2], p1[3]), bx = pk4f8(q0[0], q0[1], q0[2], q0[3]), by = pk4f8(q1[0], q1[1], q1[2], q1[3]);
;                 { auto r = __builtin_amdgcn_permlane16_swap(ax, bx, false, false); ax = r[0]; bx = r[1]; }
;                 { auto r = __builtin_amdgcn_permlane16_swap(ay, by, false, false); ay = r[0]; by = r[1]; }
;                 u32x4 w; w.x = ax; w.y = ay; w.z = bx; w.w = by;
;                 *(u32x4*)rowp = w; }
;     ...
;             PG8_WAIT_V(8); PG8_WAIT_L(0); PG8_BAR; PG8_MMA(0, 0, At, B0); PG8_MMA(0, 1, At, B1); PG8_BAR; PG8_SCHED;
;             PG8_LDA(At, 1, 1); PG8_STAGE(PG8_SB(1, 0), b3, voffB); PG8_STAGE(PG8_SB(1, 1), b3 + hstep, voffB); PG8_STAGE_A(PG8_SA(1, 0), a3, o2, 0);
;             PG8_WAIT_V(8); PG8_WAIT_L(0); PG8_BAR; PG8_MMA(1, 0, At, B0); PG8_MMA(1, 1, At, B1); PG8_BAR; PG8_SCHED;
	s_setprio 1
	s_waitcnt lgkmcnt(0)
	v_mfma_scale_f32_16x16x128_f8f6f4 v[76:79], v[158:165], v[202:209], v[76:79], v211, v212 op_sel_hi:[0,0,0]
	v_mfma_scale_f32_16x16x128_f8f6f4 v[72:75], v[166:173], v[202:209], v[72:75], v211, v212 op_sel_hi:[0,0,0]
	v_mfma_scale_f32_16x16x128_f8f6f4 v[44:47], v[158:165], v[220:227], v[44:47], v211, v212 op_sel_hi:[0,0,0]
	v_mfma_scale_f32_16x16x128_f8f6f4 v[40:43], v[166:173], v[220:227], v[40:43], v211, v212 op_sel_hi:[0,0,0]
	v_mfma_scale_f32_16x16x128_f8f6f4 v[20:23], v[158:165], v[236:243], v[20:23], v211, v212 op_sel_hi:[0,0,0]
	v_mfma_scale_f32_16x16x128_f8f6f4 v[16:19], v[166:173], v[236:243], v[16:19], v211, v212 op_sel_hi:[0,0,0]
	v_mfma_scale_f32_16x16x128_f8f6f4 v[8:11], v[158:165], v[244:251], v[8:11], v211, v212 op_sel_hi:[0,0,0]
	v_mfma_scale_f32_16x16x128_f8f6f4 v[4:7], v[166:173], v[244:251], v[4:7], v211, v212 op_sel_hi:[0,0,0]
	s_setprio 0
	s_setprio 1
	v_mfma_scale_f32_16x16x128_f8f6f4 v[92:95], v[182:189], v[202:209], v[92:95], v211, v212 op_sel_hi:[0,0,0]
	v_mfma_scale_f32_16x16x128_f8f6f4 v[88:91], v[190:197], v[202:209], v[88:91], v211, v212 op_sel_hi:[0,0,0]
	v_mfma_scale_f32_16x16x128_f8f6f4 v[60:63], v[182:189], v[220:227], v[60:63], v211, v212 op_sel_hi:[0,0,0]
	v_mfma_scale_f32_16x16x128_f8f6f4 v[56:59], v[190:197], v[220:227], v[56:59], v211, v212 op_sel_hi:[0,0,0]
	v_mfma_scale_f32_16x16x128_f8f6f4 v[28:31], v[182:189], v[236:243], v[28:31], v211, v212 op_sel_hi:[0,0,0]
	v_mfma_scale_f32_16x16x128_f8f6f4 v[24:27], v[190:197], v[236:243], v[24:27], v211, v212 op_sel_hi:[0,0,0]
	v_mfma_scale_f32_16x16x128_f8f6f4 v[12:15], v[182:189], v[244:251], v[12:15], v211, v212 op_sel_hi:[0,0,0]
	v_mfma_scale_f32_16x16x128_f8f6f4 v[0:3], v[190:197], v[244:251], v[0:3], v211, v212 op_sel_hi:[0,0,0]
	s_setprio 0
	s_barrier
	s_cmpk_lt_i32 s41, 0x480
	v_mov_b32_e32 v139, v200
	s_cselect_b32 s0, 0, 0xfffffb80
	s_mov_b32 s1, 0x18c00000
	s_cselect_b32 s1, s1, 0x2ae00000
	s_add_i32 s2, s0, s41
	v_ashrrev_i32_e32 v158, 1, v139
	s_add_u32 s0, s6, s1
	v_and_b32_e32 v138, 16, v139
	v_and_b32_e32 v158, -8, v158
	s_addc_u32 s1, s7, 0
	s_lshl_b32 s3, s42, 8
	v_add_u32_e32 v159, 0x78, v158
	v_cmp_eq_u32_e32 vcc, 0, v138
	v_and_or_b32 v139, v139, 15, v140
	s_or_b32 s3, s3, s16
	v_cndmask_b32_e32 v138, v159, v158, vcc
	v_lshl_add_u32 v158, s2, 8, v139
	s_mov_b32 s2, 0x41800000
	v_pk_mul_f32 v[162:163], v[114:115], s[2:3] op_sel_hi:[1,0]
	v_pk_mul_f32 v[114:115], v[112:113], s[2:3] op_sel_hi:[1,0]
	v_pk_mul_f32 v[116:117], v[116:117], s[2:3] op_sel_hi:[1,0]
	v_pk_mul_f32 v[124:125], v[124:125], s[2:3] op_sel_hi:[1,0]
	v_pk_mul_f32 v[120:121], v[120:121], s[2:3] op_sel_hi:[1,0]
	v_cvt_pk_fp8_f32 v113, v114, v115
	v_cvt_pk_fp8_f32 v112, v116, v117
	v_cvt_pk_fp8_f32 v114, v124, v125
	v_cvt_pk_fp8_f32 v115, v120, v121
	v_pk_mul_f32 v[118:119], v[118:119], s[2:3] op_sel_hi:[1,0]
	v_pk_mul_f32 v[126:127], v[126:127], s[2:3] op_sel_hi:[1,0]
	v_pk_mul_f32 v[122:123], v[122:123], s[2:3] op_sel_hi:[1,0]
	v_cvt_pk_fp8_f32 v112, v118, v119 op_sel:[0,0,1]
	v_cvt_pk_fp8_f32 v114, v126, v127 op_sel:[0,0,1]
	v_cvt_pk_fp8_f32 v113, v162, v163 op_sel:[0,0,1]
	v_cvt_pk_fp8_f32 v115, v122, v123 op_sel:[0,0,1]
	v_add_u32_e32 v138, s3, v138
	v_ashrrev_i32_e32 v139, 31, v138
	v_ashrrev_i32_e32 v159, 31, v158
	v_lshl_add_u64 v[160:161], s[0:1], 0, v[138:139]
	v_lshlrev_b64 v[138:139], 10, v[158:159]
	v_lshl_add_u64 v[138:139], v[160:161], 0, v[138:139]
	v_permlane16_swap_b32_e32 v112, v114
	v_permlane16_swap_b32_e32 v113, v115
	global_store_dwordx4 v[138:139], v[112:115], off
	v_pk_mul_f32 v[100:101], v[100:101], s[2:3] op_sel_hi:[1,0]
	v_pk_mul_f32 v[108:109], v[108:109], s[2:3] op_sel_hi:[1,0]
	v_pk_mul_f32 v[114:115], v[98:99], s[2:3] op_sel_hi:[1,0]
	v_pk_mul_f32 v[98:99], v[96:97], s[2:3] op_sel_hi:[1,0]
	v_pk_mul_f32 v[104:105], v[104:105], s[2:3] op_sel_hi:[1,0]
	v_cvt_pk_fp8_f32 v97, v98, v99
	v_cvt_pk_fp8_f32 v96, v100, v101
	v_cvt_pk_fp8_f32 v98, v108, v109
	v_cvt_pk_fp8_f32 v99, v104, v105
	v_pk_mul_f32 v[102:103], v[102:103], s[2:3] op_sel_hi:[1,0]
	v_pk_mul_f32 v[110:111], v[110:111], s[2:3] op_sel_hi:[1,0]
	v_pk_mul_f32 v[106:107], v[106:107], s[2:3] op_sel_hi:[1,0]
	v_cvt_pk_fp8_f32 v96, v102, v103 op_sel:[0,0,1]
	v_cvt_pk_fp8_f32 v98, v110, v111 op_sel:[0,0,1]
	v_cvt_pk_fp8_f32 v97, v114, v115 op_sel:[0,0,1]
	v_cvt_pk_fp8_f32 v99, v106, v107 op_sel:[0,0,1]
	v_or_b32_e32 v112, 16, v158
	v_ashrrev_i32_e32 v113, 31, v112
	v_lshlrev_b64 v[112:113], 10, v[112:113]
	v_lshl_add_u64 v[112:113], v[160:161], 0, v[112:113]
	v_permlane16_swap_b32_e32 v96, v98
	v_permlane16_swap_b32_e32 v97, v99
	global_store_dwordx4 v[112:113], v[96:99], off
	v_pk_mul_f32 v[68:69], v[68:69], s[2:3] op_sel_hi:[1,0]
	v_pk_mul_f32 v[84:85], v[84:85], s[2:3] op_sel_hi:[1,0]
	v_pk_mul_f32 v[98:99], v[66:67], s[2:3] op_sel_hi:[1,0]
	v_pk_mul_f32 v[66:67], v[64:65], s[2:3] op_sel_hi:[1,0]
	v_pk_mul_f32 v[80:81], v[80:81], s[2:3] op_sel_hi:[1,0]
	v_cvt_pk_fp8_f32 v65, v66, v67
	v_cvt_pk_fp8_f32 v64, v68, v69
	v_cvt_pk_fp8_f32 v66, v84, v85
	v_cvt_pk_fp8_f32 v67, v80, v81
	v_pk_mul_f32 v[70:71], v[70:71], s[2:3] op_sel_hi:[1,0]
	v_pk_mul_f32 v[86:87], v[86:87], s[2:3] op_sel_hi:[1,0]
	v_pk_mul_f32 v[82:83], v[82:83], s[2:3] op_sel_hi:[1,0]
	v_cvt_pk_fp8_f32 v64, v70, v71 op_sel:[0,0,1]
	v_cvt_pk_fp8_f32 v66, v86, v87 op_sel:[0,0,1]
	v_cvt_pk_fp8_f32 v65, v98, v99 op_sel:[0,0,1]
	v_cvt_pk_fp8_f32 v67, v82, v83 op_sel:[0,0,1]
; __device__ __forceinline__ unsigned pk4f8(float a, float b, float c, float d) { int w = 0; w = __builtin_amdgcn_cvt_pk_fp8_f32(a, b, w, false); w = __builtin_amdgcn_cvt_pk_fp8_f32(c, d, w, true); return (unsigned)w; }
;     __device__ __forceinline__ void operator()(const f32x4 (&acc)[2][2][4][2], const Unit& u, int wr, int wc, int fr, int fq) const {
;     ...
;             for (int m = 0; m < 4; ++m) { unsigned char* rowp = base + (size_t)(row0 + ai * HALF + m * 16) * ld + col0;
;                 const f32x4 p0 = acc[ai][0][m][0] * scale, p1 = acc[ai][0][m][1] * scale, q0 = acc[ai][1][m][0] * scale, q1 = acc[ai][1][m][1] * scale;
;                 unsigned ax = pk4f8(p0[0], p0[1], p0[2], p0[3]), ay = pk4f8(p1[0], p1[1], p1[2], p1[3]), bx = pk4f8(q0[0], q0[1], q0[2], q0[3]), by = pk4f8(q1[0], q1[1], q1[2], q1[3]);
;                 { auto r = __builtin_amdgcn_permlane16_swap(ax, bx, false, false); ax = r[0]; bx = r[1]; }
;                 { auto r = __builtin_amdgcn_permlane16_swap(ay, by, false, false); ay = r[0]; by = r[1]; }
;                 u32x4 w; w.x = ax; w.y = ay; w.z = bx; w.w = by;
;                 *(u32x4*)rowp = w; }
;     ...
;           E(acc, cur, wr, wc, le_ & 15, le_ >> 4); } S.done(cur);
;         if constexpr (TIMED) pg8_tm(tmisc, wid, lane, has_next ? 27 : tseg_after);
;         if (!has_next) break;
; #pragma unroll
;         for (int a = 0; a < 2; ++a)
; #pragma unroll
;             for (int b = 0; b < 2; ++b)
; #pragma unroll
;                 for (int m = 0; m < 4; ++m)
; #pragma unroll
;                     for (int n = 0; n < 2; ++n) acc[a][b][m][n] = (f32x4){0.f, 0.f, 0.f, 0.f};
;         cur = nxt; cA = nA; cB = nB; ++ui;
	v_or_b32_e32 v96, 32, v158
	v_ashrrev_i32_e32 v97, 31, v96
	v_lshlrev_b64 v[96:97], 10, v[96:97]
	v_lshl_add_u64 v[96:97], v[160:161], 0, v[96:97]
	v_permlane16_swap_b32_e32 v64, v66
	v_permlane16_swap_b32_e32 v65, v67
	global_store_dwordx4 v[96:97], v[64:67], off
	v_pk_mul_f32 v[36:37], v[36:37], s[2:3] op_sel_hi:[1,0]
	v_pk_mul_f32 v[52:53], v[52:53], s[2:3] op_sel_hi:[1,0]
	v_pk_mul_f32 v[66:67], v[34:35], s[2:3] op_sel_hi:[1,0]
	v_pk_mul_f32 v[34:35], v[32:33], s[2:3] op_sel_hi:[1,0]
	v_pk_mul_f32 v[48:49], v[48:49], s[2:3] op_sel_hi:[1,0]
	v_cvt_pk_fp8_f32 v33, v34, v35
	v_cvt_pk_fp8_f32 v32, v36, v37
	v_cvt_pk_fp8_f32 v34, v52, v53
	v_cvt_pk_fp8_f32 v35, v48, v49
	v_pk_mul_f32 v[38:39], v[38:39], s[2:3] op_sel_hi:[1,0]
	v_pk_mul_f32 v[54:55], v[54:55], s[2:3] op_sel_hi:[1,0]
	v_pk_mul_f32 v[50:51], v[50:51], s[2:3] op_sel_hi:[1,0]
	v_cvt_pk_fp8_f32 v32, v38, v39 op_sel:[0,0,1]
	v_cvt_pk_fp8_f32 v34, v54, v55 op_sel:[0,0,1]
	v_cvt_pk_fp8_f32 v33, v66, v67 op_sel:[0,0,1]
	v_cvt_pk_fp8_f32 v35, v50, v51 op_sel:[0,0,1]
	v_or_b32_e32 v64, 48, v158
	v_ashrrev_i32_e32 v65, 31, v64
	v_lshlrev_b64 v[64:65], 10, v[64:65]
	v_lshl_add_u64 v[64:65], v[160:161], 0, v[64:65]
	v_permlane16_swap_b32_e32 v32, v34
	v_permlane16_swap_b32_e32 v33, v35
	global_store_dwordx4 v[64:65], v[32:35], off
	v_pk_mul_f32 v[48:49], v[72:73], s[2:3] op_sel_hi:[1,0]
	v_pk_mul_f32 v[52:53], v[92:93], s[2:3] op_sel_hi:[1,0]
	v_pk_mul_f32 v[34:35], v[76:77], s[2:3] op_sel_hi:[1,0]
	v_pk_mul_f32 v[64:65], v[88:89], s[2:3] op_sel_hi:[1,0]
	v_cvt_pk_fp8_f32 v32, v34, v35
	v_cvt_pk_fp8_f32 v33, v48, v49
	v_cvt_pk_fp8_f32 v34, v52, v53
	v_cvt_pk_fp8_f32 v35, v64, v65
	v_pk_mul_f32 v[36:37], v[78:79], s[2:3] op_sel_hi:[1,0]
	v_pk_mul_f32 v[38:39], v[74:75], s[2:3] op_sel_hi:[1,0]
	v_pk_mul_f32 v[50:51], v[94:95], s[2:3] op_sel_hi:[1,0]
	v_pk_mul_f32 v[54:55], v[90:91], s[2:3] op_sel_hi:[1,0]
	v_cvt_pk_fp8_f32 v32, v36, v37 op_sel:[0,0,1]
	v_cvt_pk_fp8_f32 v34, v50, v51 op_sel:[0,0,1]
	v_cvt_pk_fp8_f32 v33, v38, v39 op_sel:[0,0,1]
	v_cvt_pk_fp8_f32 v35, v54, v55 op_sel:[0,0,1]
	s_mov_b32 s0, 0x20000
	v_add_co_u32_e32 v36, vcc, s0, v138
	v_permlane16_swap_b32_e32 v32, v34
	v_permlane16_swap_b32_e32 v33, v35
	v_addc_co_u32_e32 v37, vcc, 0, v139, vcc
	global_store_dwordx4 v[36:37], v[32:35], off
	v_pk_mul_f32 v[40:41], v[40:41], s[2:3] op_sel_hi:[1,0]
	v_pk_mul_f32 v[48:49], v[56:57], s[2:3] op_sel_hi:[1,0]
	v_pk_mul_f32 v[34:35], v[44:45], s[2:3] op_sel_hi:[1,0]
	v_pk_mul_f32 v[44:45], v[60:61], s[2:3] op_sel_hi:[1,0]
	v_cvt_pk_fp8_f32 v32, v34, v35
	v_cvt_pk_fp8_f32 v33, v40, v41
	v_cvt_pk_fp8_f32 v34, v44, v45
	v_cvt_pk_fp8_f32 v35, v48, v49
	v_pk_mul_f32 v[36:37], v[46:47], s[2:3] op_sel_hi:[1,0]
	v_pk_mul_f32 v[38:39], v[42:43], s[2:3] op_sel_hi:[1,0]
	v_pk_mul_f32 v[42:43], v[62:63], s[2:3] op_sel_hi:[1,0]
	v_pk_mul_f32 v[46:47], v[58:59], s[2:3] op_sel_hi:[1,0]
	v_cvt_pk_fp8_f32 v32, v36, v37 op_sel:[0,0,1]
	v_cvt_pk_fp8_f32 v34, v42, v43 op_sel:[0,0,1]
	v_cvt_pk_fp8_f32 v33, v38, v39 op_sel:[0,0,1]
	v_cvt_pk_fp8_f32 v35, v46, v47 op_sel:[0,0,1]
	s_mov_b32 s0, 0x24000
	v_add_co_u32_e32 v36, vcc, s0, v138
	v_permlane16_swap_b32_e32 v32, v34
	v_permlane16_swap_b32_e32 v33, v35
	v_addc_co_u32_e32 v37, vcc, 0, v139, vcc
	global_store_dwordx4 v[36:37], v[32:35], off
	v_pk_mul_f32 v[20:21], v[20:21], s[2:3] op_sel_hi:[1,0]
	v_pk_mul_f32 v[28:29], v[28:29], s[2:3] op_sel_hi:[1,0]
	v_pk_mul_f32 v[32:33], v[18:19], s[2:3] op_sel_hi:[1,0]
	v_pk_mul_f32 v[18:19], v[16:17], s[2:3] op_sel_hi:[1,0]
	v_pk_mul_f32 v[24:25], v[24:25], s[2:3] op_sel_hi:[1,0]
	v_cvt_pk_fp8_f32 v17, v18, v19
	v_cvt_pk_fp8_f32 v16, v20, v21
	v_cvt_pk_fp8_f32 v18, v28, v29
	v_cvt_pk_fp8_f32 v19, v24, v25
	v_pk_mul_f32 v[22:23], v[22:23], s[2:3] op_sel_hi:[1,0]
	v_pk_mul_f32 v[30:31], v[30:31], s[2:3] op_sel_hi:[1,0]
	v_pk_mul_f32 v[26:27], v[26:27], s[2:3] op_sel_hi:[1,0]
	v_cvt_pk_fp8_f32 v16, v22, v23 op_sel:[0,0,1]
	v_cvt_pk_fp8_f32 v18, v30, v31 op_sel:[0,0,1]
	v_cvt_pk_fp8_f32 v17, v32, v33 op_sel:[0,0,1]
	v_cvt_pk_fp8_f32 v19, v26, v27 op_sel:[0,0,1]
	s_mov_b32 s0, 0x28000
	v_add_co_u32_e32 v20, vcc, s0, v138
	v_permlane16_swap_b32_e32 v16, v18
	v_permlane16_swap_b32_e32 v17, v19
	v_addc_co_u32_e32 v21, vcc, 0, v139, vcc
	global_store_dwordx4 v[20:21], v[16:19], off
	v_pk_mul_f32 v[8:9], v[8:9], s[2:3] op_sel_hi:[1,0]
	v_pk_mul_f32 v[4:5], v[4:5], s[2:3] op_sel_hi:[1,0]
	v_pk_mul_f32 v[12:13], v[12:13], s[2:3] op_sel_hi:[1,0]
	v_pk_mul_f32 v[16:17], v[2:3], s[2:3] op_sel_hi:[1,0]
	v_pk_mul_f32 v[18:19], v[0:1], s[2:3] op_sel_hi:[1,0]
	v_cvt_pk_fp8_f32 v0, v8, v9
	v_cvt_pk_fp8_f32 v1, v4, v5
	v_cvt_pk_fp8_f32 v2, v12, v13
	v_cvt_pk_fp8_f32 v3, v18, v19
	v_pk_mul_f32 v[10:11], v[10:11], s[2:3] op_sel_hi:[1,0]
	v_pk_mul_f32 v[6:7], v[6:7], s[2:3] op_sel_hi:[1,0]
	v_pk_mul_f32 v[14:15], v[14:15], s[2:3] op_sel_hi:[1,0]
	v_cvt_pk_fp8_f32 v0, v10, v11 op_sel:[0,0,1]
	v_cvt_pk_fp8_f32 v2, v14, v15 op_sel:[0,0,1]
	v_cvt_pk_fp8_f32 v1, v6, v7 op_sel:[0,0,1]
	v_cvt_pk_fp8_f32 v3, v16, v17 op_sel:[0,0,1]
	v_add_co_u32_e32 v4, vcc, 0x2c000, v138
	v_permlane16_swap_b32_e32 v0, v2
	s_nop 0
	v_addc_co_u32_e32 v5, vcc, 0, v139, vcc
	v_permlane16_swap_b32_e32 v1, v3
	s_add_i32 s40, s40, 1
	s_andn2_b64 vcc, exec, s[26:27]
	s_mov_b32 s42, s22
	s_mov_b32 s41, s14
	s_mov_b64 s[0:1], s[36:37]
	global_store_dwordx4 v[4:5], v[0:3], off
	s_cbranch_vccz .LBB0_1638
